# speedup vs baseline: 1.0108x; 1.0028x over previous
.LBB3_6:
	s_or_b64 exec, exec, s[24:25]
	s_or_b32 s24, s16, 8
	s_ashr_i32 s25, s24, 31
	s_lshl_b64 s[24:25], s[24:25], 16
	s_add_u32 s9, s6, s24
	s_addc_u32 s16, s7, s25
	s_add_u32 s24, s9, s17
	s_addc_u32 s25, s16, 0
	s_add_i32 s9, 0, 0x18000
	s_add_i32 s16, s9, s31
	v_mov_b32_e32 v3, v140
	s_mov_b32 m0, s16
	v_mov_b32_e32 v130, v140
	s_waitcnt vmcnt(4)
	s_barrier
	s_add_i32 s51, s43, 0x8000
	global_load_lds_dwordx4 v3, s[24:25] sc0
	s_add_i32 m0, s16, 0x2000
	v_lshl_add_u64 v[4:5], s[24:25], 0, v[130:131]
	v_lshl_add_u64 v[4:5], v[4:5], 0, s[18:19]
	v_mov_b32_e32 v130, v1
	global_load_lds_dwordx4 v[4:5], off sc0
	s_mov_b64 s[18:19], 0x80
	v_lshl_add_u64 v[4:5], s[14:15], 0, v[130:131]
	v_lshl_add_u64 v[4:5], v[4:5], 0, s[18:19]
	s_mov_b32 m0, s51
	v_mov_b32_e32 v130, v1
	global_load_lds_dwordx4 v[4:5], off
	s_add_i32 s52, s43, 0xa000
	v_lshl_add_u64 v[4:5], s[14:15], 0, v[130:131]
	s_mov_b64 s[14:15], 0x10080
	v_lshl_add_u64 v[4:5], v[4:5], 0, s[14:15]
	s_mov_b32 m0, s52
	s_add_i32 s14, 0, 0x1c000
	v_mov_b32_e32 v130, v140
	global_load_lds_dwordx4 v[4:5], off
	s_add_i32 s15, s14, s31
	s_mov_b32 m0, s15
	v_lshl_add_u64 v[4:5], s[24:25], 0, v[130:131]
	v_lshl_add_u64 v[4:5], v[4:5], 0, s[20:21]
	v_mov_b32_e32 v130, v140
	global_load_lds_dwordx4 v[4:5], off sc0
	s_add_i32 m0, s15, 0x2000
	v_lshl_add_u64 v[4:5], s[24:25], 0, v[130:131]
	v_lshl_add_u64 v[4:5], v[4:5], 0, s[22:23]
	global_load_lds_dwordx4 v[4:5], off sc0
	v_lshlrev_b32_e32 v4, 6, v0
	v_lshlrev_b32_e32 v6, 2, v0
	v_and_b32_e32 v3, 48, v0
	v_and_b32_e32 v5, 0x3c0, v4
	v_and_b32_e32 v6, 32, v6
	v_bitop3_b32 v3, v3, v6, v5 bitop3:0x36
	v_add_u32_e32 v7, s9, v3
	s_lshl_b32 s9, s28, 3
	s_add_i32 s26, s26, s9
	s_sub_i32 s9, s26, s30
	v_add_u32_e32 v8, s14, v3
	s_sub_i32 s9, s9, s29
	s_lshl_b32 s14, s27, 3
	s_add_i32 s15, 0, 0x10000
	s_sub_i32 s9, s9, s14
	v_add_u32_e32 v5, s15, v3
	s_add_i32 s15, 0, 0x14000
	s_lshl_b32 s14, s9, 8
	v_add_u32_e32 v6, s15, v3
	s_ashr_i32 s15, s14, 31
	s_lshl_b64 s[14:15], s[14:15], 10
	s_add_u32 s4, s4, s14
	s_addc_u32 s5, s5, s15
	s_add_u32 s4, s4, 0x30100
	s_addc_u32 s5, s5, 0
	s_add_u32 s9, s12, s17
	s_addc_u32 s12, s13, 0
	s_add_u32 s6, s6, s9
	s_waitcnt vmcnt(6)
	v_lshlrev_b32_e32 v2, 13, v2
	s_addc_u32 s7, s7, s12
	s_waitcnt lgkmcnt(0)
	s_lshl_b32 s56, s8, 2
	s_add_u32 s56, s2, s56
	s_addc_u32 s57, s3, 0
	v_and_b32_e32 v254, 63, v0
	v_lshlrev_b32_e32 v254, 4, v254
	s_mov_b32 m0, 0x20000
	s_nop 0
	global_load_lds_dwordx4 v254, s[56:57]
	v_and_b32_e32 v4, 0x3000, v4
	v_add_u32_e32 v3, 0, v3
	v_or_b32_e32 v9, 0x800, v2
	v_or_b32_e32 v10, 0x1000, v2
	v_or_b32_e32 v11, 0x1800, v2
	s_add_u32 s6, s6, 0x180c00
	s_mov_b32 s12, 0xfffeff80
	s_movk_i32 s14, 0xff80
	s_mov_b32 s16, 0xfff7f400
	s_mov_b32 s18, 0xfff7f800
	s_mov_b32 s20, 0xfffd0000
	s_mov_b32 s22, 0xfffe0000
	s_mov_b32 s24, 0xfff7fc00
	s_mov_b32 s26, 0xfff80000
	s_mov_b32 s28, 0xffff0000
	s_movk_i32 s30, 0xf400
	s_movk_i32 s34, 0xf800
	s_mov_b32 s36, 0xfffd0080
	s_mov_b32 s38, 0xfffe0080
	s_movk_i32 s40, 0xfc00
	s_addc_u32 s7, s7, 0
	s_mov_b32 s53, -2
	v_add_u32_e32 v132, v5, v4
	v_add_u32_e32 v133, v3, v2
	v_add_u32_e32 v134, v3, v9
	v_add_u32_e32 v135, v3, v10
	v_add_u32_e32 v136, v3, v11
	s_mov_b32 s13, -1
	s_add_i32 s9, s43, 0xc000
	s_mov_b32 s15, -1
	s_add_i32 s42, s43, 0xe000
	v_add_u32_e32 v137, v6, v4
	s_mov_b32 s17, -1
	s_mov_b32 s19, -1
	s_mov_b32 s21, -1
	s_mov_b32 s23, -1
	s_mov_b32 s25, -1
	s_mov_b32 s27, -1
	v_add_u32_e32 v138, v7, v4
	s_mov_b32 s29, -1
	v_add_u32_e32 v139, v8, v4
	s_mov_b32 s31, -1
	s_mov_b32 s35, -1
	s_add_i32 s54, s43, 0x1a000
	s_mov_b32 s37, -1
	s_mov_b32 s39, -1
	s_mov_b32 s41, -1
	s_add_i32 s55, s43, 0x1e000
	v_mov_b32_e32 v2, v131
	v_mov_b32_e32 v3, v131
	v_mov_b32_e32 v4, v131
	v_mov_b32_e32 v5, v131
	v_mov_b32_e32 v10, v131
	v_mov_b32_e32 v11, v131
	v_mov_b32_e32 v12, v131
	v_mov_b32_e32 v13, v131
	v_mov_b32_e32 v6, v131
	v_mov_b32_e32 v7, v131
	v_mov_b32_e32 v8, v131
	v_mov_b32_e32 v9, v131
	v_mov_b32_e32 v14, v131
	v_mov_b32_e32 v15, v131
	v_mov_b32_e32 v16, v131
	v_mov_b32_e32 v17, v131
	v_mov_b32_e32 v30, v131
	v_mov_b32_e32 v31, v131
	v_mov_b32_e32 v32, v131
	v_mov_b32_e32 v33, v131
	v_mov_b32_e32 v42, v131
	v_mov_b32_e32 v43, v131
	v_mov_b32_e32 v44, v131
	v_mov_b32_e32 v45, v131
	v_mov_b32_e32 v38, v131
	v_mov_b32_e32 v39, v131
	v_mov_b32_e32 v40, v131
	v_mov_b32_e32 v41, v131
	v_mov_b32_e32 v46, v131
	v_mov_b32_e32 v47, v131
	v_mov_b32_e32 v48, v131
	v_mov_b32_e32 v49, v131
	v_mov_b32_e32 v18, v131
	v_mov_b32_e32 v19, v131
	v_mov_b32_e32 v20, v131
	v_mov_b32_e32 v21, v131
	v_mov_b32_e32 v26, v131
	v_mov_b32_e32 v27, v131
	v_mov_b32_e32 v28, v131
	v_mov_b32_e32 v29, v131
	v_mov_b32_e32 v22, v131
	v_mov_b32_e32 v23, v131
	v_mov_b32_e32 v24, v131
	v_mov_b32_e32 v25, v131
	v_mov_b32_e32 v34, v131
	v_mov_b32_e32 v35, v131
	v_mov_b32_e32 v36, v131
	v_mov_b32_e32 v37, v131
	v_mov_b32_e32 v50, v131
	v_mov_b32_e32 v51, v131
	v_mov_b32_e32 v52, v131
	v_mov_b32_e32 v53, v131
	v_mov_b32_e32 v58, v131
	v_mov_b32_e32 v59, v131
	v_mov_b32_e32 v60, v131
	v_mov_b32_e32 v61, v131
	v_mov_b32_e32 v54, v131
	v_mov_b32_e32 v55, v131
	v_mov_b32_e32 v56, v131
	v_mov_b32_e32 v57, v131
	v_mov_b32_e32 v62, v131
	v_mov_b32_e32 v63, v131
	v_mov_b32_e32 v64, v131
	v_mov_b32_e32 v65, v131
	v_mov_b32_e32 v66, v131
	v_mov_b32_e32 v67, v131
	v_mov_b32_e32 v68, v131
	v_mov_b32_e32 v69, v131
	v_mov_b32_e32 v74, v131
	v_mov_b32_e32 v75, v131
	v_mov_b32_e32 v76, v131
	v_mov_b32_e32 v77, v131
	v_mov_b32_e32 v70, v131
	v_mov_b32_e32 v71, v131
	v_mov_b32_e32 v72, v131
	v_mov_b32_e32 v73, v131
	v_mov_b32_e32 v78, v131
	v_mov_b32_e32 v79, v131
	v_mov_b32_e32 v80, v131
	v_mov_b32_e32 v81, v131
	v_mov_b32_e32 v98, v131
	v_mov_b32_e32 v99, v131
	v_mov_b32_e32 v100, v131
	v_mov_b32_e32 v101, v131
	v_mov_b32_e32 v106, v131
	v_mov_b32_e32 v107, v131
	v_mov_b32_e32 v108, v131
	v_mov_b32_e32 v109, v131
	v_mov_b32_e32 v102, v131
	v_mov_b32_e32 v103, v131
	v_mov_b32_e32 v104, v131
	v_mov_b32_e32 v105, v131
	v_mov_b32_e32 v110, v131
	v_mov_b32_e32 v111, v131
	v_mov_b32_e32 v112, v131
	v_mov_b32_e32 v113, v131
	v_mov_b32_e32 v82, v131
	v_mov_b32_e32 v83, v131
	v_mov_b32_e32 v84, v131
	v_mov_b32_e32 v85, v131
	v_mov_b32_e32 v90, v131
	v_mov_b32_e32 v91, v131
	v_mov_b32_e32 v92, v131
	v_mov_b32_e32 v93, v131
	v_mov_b32_e32 v86, v131
	v_mov_b32_e32 v87, v131
	v_mov_b32_e32 v88, v131
	v_mov_b32_e32 v89, v131
	v_mov_b32_e32 v94, v131
	v_mov_b32_e32 v95, v131
	v_mov_b32_e32 v96, v131
	v_mov_b32_e32 v97, v131
	v_mov_b32_e32 v114, v131
	v_mov_b32_e32 v115, v131
	v_mov_b32_e32 v116, v131
	v_mov_b32_e32 v117, v131
	v_mov_b32_e32 v118, v131
	v_mov_b32_e32 v119, v131
	v_mov_b32_e32 v120, v131
	v_mov_b32_e32 v121, v131
	v_mov_b32_e32 v122, v131
	v_mov_b32_e32 v123, v131
	v_mov_b32_e32 v124, v131
	v_mov_b32_e32 v125, v131
	v_mov_b32_e32 v126, v131
	v_mov_b32_e32 v127, v131
	v_mov_b32_e32 v128, v131
	v_mov_b32_e32 v129, v131
	s_barrier

.LBB3_13:
	s_or_b64 exec, exec, s[4:5]
	v_mov_b32_e32 v172, 0
	v_ashrrev_i32_e32 v1, 2, v0
	v_and_b32_e32 v1, 0xffffffc0, v1
	v_add_u32_e32 v1, s8, v1
	v_lshrrev_b32_e32 v130, 2, v0
	v_and_or_b32 v156, v130, 12, v1
	v_ashrrev_i32_e32 v157, 31, v156
	v_lshl_add_u64 v[150:151], v[156:157], 2, s[2:3]
	v_lshrrev_b32_e32 v254, 8, v0
	v_bfe_u32 v255, v0, 4, 2
	v_lshlrev_b32_e32 v254, 8, v254
	v_lshl_add_u32 v254, v255, 4, v254
	v_add_u32_e32 v254, 0x20000, v254
	ds_read_b128 v[138:141], v254
	ds_read_b128 v[142:145], v254 offset:64
	v_and_b32_e32 v130, 15, v0
	v_and_b32_e32 v180, 1, v0
	v_lshrrev_b32_e32 v0, 1, v0
	v_and_b32_e32 v131, 0x60, v0
	s_movk_i32 s3, 0xff6e
	v_lshl_or_b32 v131, s33, 8, v131
	v_lshlrev_b32_e32 v0, 4, v180
	v_or_b32_e32 v181, v131, v130
	v_bitop3_b32 v158, v131, s3, v130 bitop3:0xc8
	v_or_b32_e32 v130, v0, v156
	v_or_b32_e32 v132, 1, v181
	v_or_b32_e32 v134, 16, v158
	v_or_b32_e32 v136, 17, v181
	v_ashrrev_i32_e32 v131, 31, v130
	v_ashrrev_i32_e32 v133, 31, v132
	v_ashrrev_i32_e32 v135, 31, v134
	v_ashrrev_i32_e32 v137, 31, v136
	v_lshl_add_u64 v[160:161], v[130:131], 2, s[0:1]
	v_lshlrev_b64 v[152:153], 12, v[132:133]
	v_lshlrev_b64 v[148:149], 12, v[134:135]
	v_lshlrev_b64 v[146:147], 12, v[136:137]
	ds_read_b128 v[130:133], v254 offset:128
	ds_read_b128 v[134:137], v254 offset:192
	ds_read_b128 v[184:187], v254 offset:576
	ds_read_b128 v[188:191], v254 offset:512
	ds_read_b128 v[192:195], v254 offset:640
	ds_read_b128 v[196:199], v254 offset:704
	s_mov_b32 s2, 0x34800000
	v_cmp_eq_u32_e32 vcc, 0, v180
	v_mov_b32_e32 v173, 0
	v_mov_b32_e32 v174, 0
	v_mov_b32_e32 v175, 0
	v_ashrrev_i32_e32 v159, 31, v158
	v_mov_b32_e32 v176, 0
	v_mov_b32_e32 v177, 0
	v_mov_b32_e32 v178, 0
	v_mov_b32_e32 v179, 0
	v_lshlrev_b64 v[154:155], 12, v[158:159]
	v_lshl_add_u64 v[162:163], v[160:161], 0, v[154:155]
	v_lshl_add_u64 v[164:165], v[160:161], 0, v[152:153]
	v_lshl_add_u64 v[166:167], v[160:161], 0, v[148:149]
	v_mov_b32_e32 v1, 0
	s_waitcnt vmcnt(0) lgkmcnt(0)
	v_pk_fma_f32 v[128:129], v[128:129], s[2:3], v[140:141] op_sel_hi:[1,0,1]
	v_pk_fma_f32 v[126:127], v[126:127], s[2:3], v[138:139] op_sel_hi:[1,0,1]
	v_pk_fma_f32 v[120:121], v[120:121], s[2:3], v[144:145] op_sel_hi:[1,0,1]
	v_pk_fma_f32 v[118:119], v[118:119], s[2:3], v[142:143] op_sel_hi:[1,0,1]
	v_pk_fma_f32 v[124:125], v[124:125], s[2:3], v[140:141] op_sel_hi:[1,0,1]
	v_pk_fma_f32 v[122:123], v[122:123], s[2:3], v[138:139] op_sel_hi:[1,0,1]
	v_pk_fma_f32 v[168:169], v[116:117], s[2:3], v[144:145] op_sel_hi:[1,0,1]
	v_pk_fma_f32 v[170:171], v[114:115], s[2:3], v[142:143] op_sel_hi:[1,0,1]
	v_cndmask_b32_e32 v114, v129, v121, vcc
	v_cndmask_b32_e32 v115, v128, v120, vcc
	v_cndmask_b32_e32 v116, v127, v119, vcc
	v_cndmask_b32_e32 v117, v126, v118, vcc
	v_cndmask_b32_e32 v159, v125, v169, vcc
	v_cndmask_b32_e32 v180, v124, v168, vcc
	v_cndmask_b32_e32 v182, v123, v171, vcc
	v_cndmask_b32_e32 v183, v122, v170, vcc
	v_mov_b32_dpp v172, v117 quad_perm:[1,0,3,2] row_mask:0xf bank_mask:0xf
	v_mov_b32_dpp v173, v116 quad_perm:[1,0,3,2] row_mask:0xf bank_mask:0xf
	v_mov_b32_dpp v174, v115 quad_perm:[1,0,3,2] row_mask:0xf bank_mask:0xf
	v_mov_b32_dpp v175, v114 quad_perm:[1,0,3,2] row_mask:0xf bank_mask:0xf
	v_mov_b32_dpp v176, v183 quad_perm:[1,0,3,2] row_mask:0xf bank_mask:0xf
	v_mov_b32_dpp v177, v182 quad_perm:[1,0,3,2] row_mask:0xf bank_mask:0xf
	v_mov_b32_dpp v178, v180 quad_perm:[1,0,3,2] row_mask:0xf bank_mask:0xf
	v_mov_b32_dpp v179, v159 quad_perm:[1,0,3,2] row_mask:0xf bank_mask:0xf
	v_cndmask_b32_e32 v117, v175, v129, vcc
	v_cndmask_b32_e32 v116, v174, v128, vcc
	v_cndmask_b32_e32 v115, v173, v127, vcc
	v_cndmask_b32_e32 v114, v172, v126, vcc
	v_cndmask_b32_e32 v119, v119, v173, vcc
	v_pk_fma_f32 v[110:111], v[110:111], s[2:3], v[138:139] op_sel_hi:[1,0,1]
	v_pk_fma_f32 v[106:107], v[106:107], s[2:3], v[142:143] op_sel_hi:[1,0,1]
	v_cndmask_b32_e32 v121, v121, v175, vcc
	v_cndmask_b32_e32 v120, v120, v174, vcc
	v_cndmask_b32_e32 v118, v118, v172, vcc
	v_cndmask_b32_e32 v125, v179, v125, vcc
	v_cndmask_b32_e32 v124, v178, v124, vcc
	v_cndmask_b32_e32 v123, v177, v123, vcc
	v_cndmask_b32_e32 v122, v176, v122, vcc
	v_cndmask_b32_e32 v129, v169, v179, vcc
	v_cndmask_b32_e32 v128, v168, v178, vcc
	v_cndmask_b32_e32 v127, v171, v177, vcc
	v_cndmask_b32_e32 v126, v170, v176, vcc
	global_store_dwordx4 v[162:163], v[114:117], off
	global_store_dwordx4 v[164:165], v[118:121], off
	global_store_dwordx4 v[166:167], v[122:125], off
	v_lshl_add_u64 v[114:115], v[160:161], 0, v[146:147]
	v_pk_fma_f32 v[112:113], v[112:113], s[2:3], v[140:141] op_sel_hi:[1,0,1]
	v_pk_fma_f32 v[108:109], v[108:109], s[2:3], v[144:145] op_sel_hi:[1,0,1]
	v_cndmask_b32_e32 v116, v111, v107, vcc
	v_mov_b32_e32 v119, 0
	global_store_dwordx4 v[114:115], v[126:129], off
	v_cndmask_b32_e32 v115, v112, v108, vcc
	v_cndmask_b32_e32 v117, v110, v106, vcc
	v_mov_b32_e32 v118, 0
	v_mov_b32_dpp v119, v116 quad_perm:[1,0,3,2] row_mask:0xf bank_mask:0xf
	v_mov_b32_e32 v116, 0
	v_cndmask_b32_e32 v114, v113, v109, vcc
	v_mov_b32_dpp v118, v117 quad_perm:[1,0,3,2] row_mask:0xf bank_mask:0xf
	v_mov_b32_dpp v116, v115 quad_perm:[1,0,3,2] row_mask:0xf bank_mask:0xf
	v_mov_b32_e32 v115, 0
	v_cndmask_b32_e32 v112, v116, v112, vcc
	v_cndmask_b32_e32 v116, v108, v116, vcc
	v_mov_b32_dpp v115, v114 quad_perm:[1,0,3,2] row_mask:0xf bank_mask:0xf
	v_cndmask_b32_e32 v114, v106, v118, vcc
	v_or_b32_e32 v106, 0x80, v158
	v_cndmask_b32_e32 v113, v115, v113, vcc
	v_cndmask_b32_e32 v117, v109, v115, vcc
	v_cndmask_b32_e32 v115, v107, v119, vcc
	v_ashrrev_i32_e32 v107, 31, v106
	v_lshlrev_b64 v[108:109], 12, v[106:107]
	v_cndmask_b32_e32 v111, v119, v111, vcc
	v_cndmask_b32_e32 v110, v118, v110, vcc
	v_lshl_add_u64 v[106:107], v[160:161], 0, v[108:109]
	global_store_dwordx4 v[106:107], v[110:113], off
	v_or_b32_e32 v106, 0x81, v181
	v_ashrrev_i32_e32 v107, 31, v106
	v_lshlrev_b64 v[106:107], 12, v[106:107]
	v_lshl_add_u64 v[110:111], v[160:161], 0, v[106:107]
	v_pk_fma_f32 v[102:103], v[102:103], s[2:3], v[138:139] op_sel_hi:[1,0,1]
	v_pk_fma_f32 v[98:99], v[98:99], s[2:3], v[142:143] op_sel_hi:[1,0,1]
	global_store_dwordx4 v[110:111], v[114:117], off
	v_pk_fma_f32 v[104:105], v[104:105], s[2:3], v[140:141] op_sel_hi:[1,0,1]
	v_pk_fma_f32 v[100:101], v[100:101], s[2:3], v[144:145] op_sel_hi:[1,0,1]
	v_cndmask_b32_e32 v112, v103, v99, vcc
	v_mov_b32_e32 v115, 0
	v_cndmask_b32_e32 v111, v104, v100, vcc
	v_cndmask_b32_e32 v113, v102, v98, vcc
	v_mov_b32_e32 v114, 0
	v_mov_b32_dpp v115, v112 quad_perm:[1,0,3,2] row_mask:0xf bank_mask:0xf
	v_mov_b32_e32 v112, 0
	v_cndmask_b32_e32 v110, v105, v101, vcc
	v_mov_b32_dpp v114, v113 quad_perm:[1,0,3,2] row_mask:0xf bank_mask:0xf
	v_mov_b32_dpp v112, v111 quad_perm:[1,0,3,2] row_mask:0xf bank_mask:0xf
	v_mov_b32_e32 v111, 0
	v_cndmask_b32_e32 v104, v112, v104, vcc
	v_cndmask_b32_e32 v112, v100, v112, vcc
	v_mov_b32_dpp v111, v110 quad_perm:[1,0,3,2] row_mask:0xf bank_mask:0xf
	v_cndmask_b32_e32 v110, v98, v114, vcc
	v_or_b32_e32 v98, 0x90, v158
	v_cndmask_b32_e32 v105, v111, v105, vcc
	v_cndmask_b32_e32 v113, v101, v111, vcc
	v_cndmask_b32_e32 v111, v99, v115, vcc
	v_ashrrev_i32_e32 v99, 31, v98
	v_lshlrev_b64 v[100:101], 12, v[98:99]
	v_cndmask_b32_e32 v103, v115, v103, vcc
	v_cndmask_b32_e32 v102, v114, v102, vcc
	v_lshl_add_u64 v[98:99], v[160:161], 0, v[100:101]
	global_store_dwordx4 v[98:99], v[102:105], off
	v_or_b32_e32 v98, 0x91, v181
	v_ashrrev_i32_e32 v99, 31, v98
	v_lshlrev_b64 v[98:99], 12, v[98:99]
	v_lshl_add_u64 v[102:103], v[160:161], 0, v[98:99]
	global_store_dwordx4 v[102:103], v[110:113], off
	v_pk_fma_f32 v[96:97], v[96:97], s[2:3], v[132:133] op_sel_hi:[1,0,1]
	v_pk_fma_f32 v[94:95], v[94:95], s[2:3], v[130:131] op_sel_hi:[1,0,1]
	v_pk_fma_f32 v[104:105], v[92:93], s[2:3], v[136:137] op_sel_hi:[1,0,1]
	v_pk_fma_f32 v[110:111], v[90:91], s[2:3], v[134:135] op_sel_hi:[1,0,1]
	v_lshl_add_u64 v[102:103], v[0:1], 0, v[156:157]
	v_cndmask_b32_e32 v90, v97, v105, vcc
	v_cndmask_b32_e32 v91, v96, v104, vcc
	v_cndmask_b32_e32 v92, v95, v111, vcc
	v_cndmask_b32_e32 v93, v94, v110, vcc
	v_mov_b32_e32 v112, v1
	v_mov_b32_e32 v113, v1
	v_mov_b32_e32 v114, v1
	v_mov_b32_e32 v115, v1
	v_lshl_add_u64 v[102:103], v[102:103], 2, s[0:1]
	v_mov_b32_dpp v112, v93 quad_perm:[1,0,3,2] row_mask:0xf bank_mask:0xf
	v_mov_b32_dpp v113, v92 quad_perm:[1,0,3,2] row_mask:0xf bank_mask:0xf
	v_mov_b32_dpp v114, v91 quad_perm:[1,0,3,2] row_mask:0xf bank_mask:0xf
	v_mov_b32_dpp v115, v90 quad_perm:[1,0,3,2] row_mask:0xf bank_mask:0xf
	v_cndmask_b32_e32 v93, v115, v97, vcc
	v_cndmask_b32_e32 v92, v114, v96, vcc
	v_cndmask_b32_e32 v91, v113, v95, vcc
	v_cndmask_b32_e32 v90, v112, v94, vcc
	v_cndmask_b32_e32 v97, v105, v115, vcc
	v_cndmask_b32_e32 v96, v104, v114, vcc
	v_lshl_add_u64 v[104:105], v[102:103], 0, v[154:155]
	v_cndmask_b32_e32 v95, v111, v113, vcc
	v_cndmask_b32_e32 v94, v110, v112, vcc
	global_store_dwordx4 v[104:105], v[90:93], off offset:128
	v_pk_fma_f32 v[104:105], v[82:83], s[2:3], v[134:135] op_sel_hi:[1,0,1]
	v_mov_b32_e32 v111, v1
	v_lshl_add_u64 v[90:91], v[102:103], 0, v[152:153]
	global_store_dwordx4 v[90:91], v[94:97], off offset:128
	v_pk_fma_f32 v[90:91], v[88:89], s[2:3], v[132:133] op_sel_hi:[1,0,1]
	v_mov_b32_e32 v112, v1
	v_pk_fma_f32 v[94:95], v[86:87], s[2:3], v[130:131] op_sel_hi:[1,0,1]
	v_pk_fma_f32 v[96:97], v[84:85], s[2:3], v[136:137] op_sel_hi:[1,0,1]
	v_cndmask_b32_e32 v82, v94, v104, vcc
	s_nop 0
	v_cndmask_b32_e32 v110, v95, v105, vcc
	v_mov_b32_dpp v111, v82 quad_perm:[1,0,3,2] row_mask:0xf bank_mask:0xf
	s_nop 0
	v_cndmask_b32_e32 v92, v91, v97, vcc
	v_cndmask_b32_e32 v93, v90, v96, vcc
	v_mov_b32_dpp v112, v110 quad_perm:[1,0,3,2] row_mask:0xf bank_mask:0xf
	v_mov_b32_e32 v110, v1
	v_mov_b32_e32 v113, v1
	v_pk_fma_f32 v[80:81], v[80:81], s[2:3], v[132:133] op_sel_hi:[1,0,1]
	v_mov_b32_dpp v110, v93 quad_perm:[1,0,3,2] row_mask:0xf bank_mask:0xf
	v_mov_b32_dpp v113, v92 quad_perm:[1,0,3,2] row_mask:0xf bank_mask:0xf
	v_cndmask_b32_e32 v93, v113, v91, vcc
	v_cndmask_b32_e32 v92, v110, v90, vcc
	v_cndmask_b32_e32 v91, v112, v95, vcc
	v_cndmask_b32_e32 v90, v111, v94, vcc
	v_cndmask_b32_e32 v95, v105, v112, vcc
	v_cndmask_b32_e32 v94, v104, v111, vcc
	v_lshl_add_u64 v[104:105], v[102:103], 0, v[148:149]
	v_cndmask_b32_e32 v97, v97, v113, vcc
	v_cndmask_b32_e32 v96, v96, v110, vcc
	global_store_dwordx4 v[104:105], v[90:93], off offset:128
	v_pk_fma_f32 v[78:79], v[78:79], s[2:3], v[130:131] op_sel_hi:[1,0,1]
	v_pk_fma_f32 v[72:73], v[72:73], s[2:3], v[132:133] op_sel_hi:[1,0,1]
	v_lshl_add_u64 v[90:91], v[102:103], 0, v[146:147]
	global_store_dwordx4 v[90:91], v[94:97], off offset:128
	v_pk_fma_f32 v[90:91], v[76:77], s[2:3], v[136:137] op_sel_hi:[1,0,1]
	v_pk_fma_f32 v[92:93], v[74:75], s[2:3], v[134:135] op_sel_hi:[1,0,1]
	v_cndmask_b32_e32 v74, v81, v91, vcc
	v_cndmask_b32_e32 v75, v80, v90, vcc
	v_cndmask_b32_e32 v76, v79, v93, vcc
	v_cndmask_b32_e32 v77, v78, v92, vcc
	v_mov_b32_e32 v94, v1
	v_mov_b32_e32 v95, v1
	v_mov_b32_e32 v96, v1
	v_mov_b32_e32 v97, v1
	v_mov_b32_dpp v94, v77 quad_perm:[1,0,3,2] row_mask:0xf bank_mask:0xf
	v_mov_b32_dpp v95, v76 quad_perm:[1,0,3,2] row_mask:0xf bank_mask:0xf
	v_mov_b32_dpp v96, v75 quad_perm:[1,0,3,2] row_mask:0xf bank_mask:0xf
	v_mov_b32_dpp v97, v74 quad_perm:[1,0,3,2] row_mask:0xf bank_mask:0xf
	v_cndmask_b32_e32 v77, v97, v81, vcc
	v_cndmask_b32_e32 v76, v96, v80, vcc
	v_cndmask_b32_e32 v75, v95, v79, vcc
	v_cndmask_b32_e32 v74, v94, v78, vcc
	v_cndmask_b32_e32 v81, v91, v97, vcc
	v_cndmask_b32_e32 v80, v90, v96, vcc
	v_lshl_add_u64 v[90:91], v[102:103], 0, v[108:109]
	v_cndmask_b32_e32 v79, v93, v95, vcc
	v_cndmask_b32_e32 v78, v92, v94, vcc
	global_store_dwordx4 v[90:91], v[74:77], off offset:128
	v_pk_fma_f32 v[70:71], v[70:71], s[2:3], v[130:131] op_sel_hi:[1,0,1]
	s_nop 0
	v_pk_fma_f32 v[64:65], v[64:65], s[2:3], v[190:191] op_sel_hi:[1,0,1]
	v_lshl_add_u64 v[74:75], v[102:103], 0, v[106:107]
	global_store_dwordx4 v[74:75], v[78:81], off offset:128
	v_pk_fma_f32 v[74:75], v[68:69], s[2:3], v[136:137] op_sel_hi:[1,0,1]
	v_pk_fma_f32 v[76:77], v[66:67], s[2:3], v[134:135] op_sel_hi:[1,0,1]
	v_cndmask_b32_e32 v66, v73, v75, vcc
	v_cndmask_b32_e32 v67, v72, v74, vcc
	v_cndmask_b32_e32 v68, v71, v77, vcc
	v_cndmask_b32_e32 v69, v70, v76, vcc
	v_mov_b32_e32 v78, v1
	v_mov_b32_e32 v79, v1
	v_mov_b32_e32 v80, v1
	v_mov_b32_e32 v81, v1
	v_mov_b32_dpp v78, v69 quad_perm:[1,0,3,2] row_mask:0xf bank_mask:0xf
	v_mov_b32_dpp v79, v68 quad_perm:[1,0,3,2] row_mask:0xf bank_mask:0xf
	v_mov_b32_dpp v80, v67 quad_perm:[1,0,3,2] row_mask:0xf bank_mask:0xf
	v_mov_b32_dpp v81, v66 quad_perm:[1,0,3,2] row_mask:0xf bank_mask:0xf
	v_cndmask_b32_e32 v69, v81, v73, vcc
	v_cndmask_b32_e32 v68, v80, v72, vcc
	v_cndmask_b32_e32 v67, v79, v71, vcc
	v_cndmask_b32_e32 v66, v78, v70, vcc
	v_cndmask_b32_e32 v73, v75, v81, vcc
	v_cndmask_b32_e32 v72, v74, v80, vcc
	v_lshl_add_u64 v[74:75], v[102:103], 0, v[100:101]
	v_cndmask_b32_e32 v71, v77, v79, vcc
	v_cndmask_b32_e32 v70, v76, v78, vcc
	global_store_dwordx4 v[74:75], v[66:69], off offset:128
	v_pk_fma_f32 v[62:63], v[62:63], s[2:3], v[188:189] op_sel_hi:[1,0,1]
	v_mov_b32_e32 v74, v1
	v_lshl_add_u64 v[66:67], v[102:103], 0, v[98:99]
	global_store_dwordx4 v[66:67], v[70:73], off offset:128
	v_add_u32_e32 v66, 0x80, v156
	v_or_b32_e32 v68, v0, v66
	v_pk_fma_f32 v[70:71], v[60:61], s[2:3], v[186:187] op_sel_hi:[1,0,1]
	v_pk_fma_f32 v[72:73], v[58:59], s[2:3], v[184:185] op_sel_hi:[1,0,1]
	v_ashrrev_i32_e32 v69, 31, v68
	v_cndmask_b32_e32 v58, v65, v71, vcc
	v_cndmask_b32_e32 v59, v64, v70, vcc
	v_cndmask_b32_e32 v60, v63, v73, vcc
	v_cndmask_b32_e32 v61, v62, v72, vcc
	v_mov_b32_e32 v67, v1
	v_mov_b32_e32 v75, v1
	v_mov_b32_e32 v76, v1
	v_lshl_add_u64 v[68:69], v[68:69], 2, s[0:1]
	v_mov_b32_dpp v67, v61 quad_perm:[1,0,3,2] row_mask:0xf bank_mask:0xf
	v_mov_b32_dpp v74, v60 quad_perm:[1,0,3,2] row_mask:0xf bank_mask:0xf
	v_mov_b32_dpp v75, v59 quad_perm:[1,0,3,2] row_mask:0xf bank_mask:0xf
	v_mov_b32_dpp v76, v58 quad_perm:[1,0,3,2] row_mask:0xf bank_mask:0xf
	v_cndmask_b32_e32 v61, v76, v65, vcc
	v_cndmask_b32_e32 v60, v75, v64, vcc
	v_cndmask_b32_e32 v59, v74, v63, vcc
	v_cndmask_b32_e32 v58, v67, v62, vcc
	v_cndmask_b32_e32 v65, v71, v76, vcc
	v_cndmask_b32_e32 v64, v70, v75, vcc
	v_lshl_add_u64 v[70:71], v[68:69], 0, v[154:155]
	v_cndmask_b32_e32 v63, v73, v74, vcc
	v_cndmask_b32_e32 v62, v72, v67, vcc
	global_store_dwordx4 v[70:71], v[58:61], off
	v_pk_fma_f32 v[70:71], v[50:51], s[2:3], v[184:185] op_sel_hi:[1,0,1]
	v_mov_b32_e32 v72, v1
	v_lshl_add_u64 v[58:59], v[68:69], 0, v[152:153]
	global_store_dwordx4 v[58:59], v[62:65], off
	v_pk_fma_f32 v[58:59], v[56:57], s[2:3], v[190:191] op_sel_hi:[1,0,1]
	v_mov_b32_e32 v73, v1
	v_pk_fma_f32 v[62:63], v[54:55], s[2:3], v[188:189] op_sel_hi:[1,0,1]
	v_pk_fma_f32 v[64:65], v[52:53], s[2:3], v[186:187] op_sel_hi:[1,0,1]
	v_cndmask_b32_e32 v54, v62, v70, vcc
	s_nop 0
	v_cndmask_b32_e32 v67, v63, v71, vcc
	v_mov_b32_dpp v72, v54 quad_perm:[1,0,3,2] row_mask:0xf bank_mask:0xf
	s_nop 0
	v_cndmask_b32_e32 v60, v59, v65, vcc
	v_cndmask_b32_e32 v61, v58, v64, vcc
	v_mov_b32_dpp v73, v67 quad_perm:[1,0,3,2] row_mask:0xf bank_mask:0xf
	v_mov_b32_e32 v67, v1
	v_mov_b32_e32 v74, v1
	v_pk_fma_f32 v[48:49], v[48:49], s[2:3], v[190:191] op_sel_hi:[1,0,1]
	v_mov_b32_dpp v67, v61 quad_perm:[1,0,3,2] row_mask:0xf bank_mask:0xf
	v_mov_b32_dpp v74, v60 quad_perm:[1,0,3,2] row_mask:0xf bank_mask:0xf
	v_cndmask_b32_e32 v61, v74, v59, vcc
	v_cndmask_b32_e32 v60, v67, v58, vcc
	v_cndmask_b32_e32 v59, v73, v63, vcc
	v_cndmask_b32_e32 v58, v72, v62, vcc
	v_cndmask_b32_e32 v63, v71, v73, vcc
	v_cndmask_b32_e32 v62, v70, v72, vcc
	v_lshl_add_u64 v[70:71], v[68:69], 0, v[148:149]
	v_cndmask_b32_e32 v65, v65, v74, vcc
	v_cndmask_b32_e32 v64, v64, v67, vcc
	global_store_dwordx4 v[70:71], v[58:61], off
	v_pk_fma_f32 v[46:47], v[46:47], s[2:3], v[188:189] op_sel_hi:[1,0,1]
	v_pk_fma_f32 v[40:41], v[40:41], s[2:3], v[190:191] op_sel_hi:[1,0,1]
	v_lshl_add_u64 v[58:59], v[68:69], 0, v[146:147]
	global_store_dwordx4 v[58:59], v[62:65], off
	v_pk_fma_f32 v[58:59], v[44:45], s[2:3], v[186:187] op_sel_hi:[1,0,1]
	v_pk_fma_f32 v[60:61], v[42:43], s[2:3], v[184:185] op_sel_hi:[1,0,1]
	v_cndmask_b32_e32 v42, v49, v59, vcc
	v_cndmask_b32_e32 v43, v48, v58, vcc
	v_cndmask_b32_e32 v44, v47, v61, vcc
	v_cndmask_b32_e32 v45, v46, v60, vcc
	v_mov_b32_e32 v62, v1
	v_mov_b32_e32 v63, v1
	v_mov_b32_e32 v64, v1
	v_mov_b32_e32 v65, v1
	v_mov_b32_dpp v62, v45 quad_perm:[1,0,3,2] row_mask:0xf bank_mask:0xf
	v_mov_b32_dpp v63, v44 quad_perm:[1,0,3,2] row_mask:0xf bank_mask:0xf
	v_mov_b32_dpp v64, v43 quad_perm:[1,0,3,2] row_mask:0xf bank_mask:0xf
	v_mov_b32_dpp v65, v42 quad_perm:[1,0,3,2] row_mask:0xf bank_mask:0xf
	v_cndmask_b32_e32 v45, v65, v49, vcc
	v_cndmask_b32_e32 v44, v64, v48, vcc
	v_cndmask_b32_e32 v43, v63, v47, vcc
	v_cndmask_b32_e32 v42, v62, v46, vcc
	v_cndmask_b32_e32 v49, v59, v65, vcc
	v_cndmask_b32_e32 v48, v58, v64, vcc
	v_lshl_add_u64 v[58:59], v[68:69], 0, v[108:109]
	v_cndmask_b32_e32 v47, v61, v63, vcc
	v_cndmask_b32_e32 v46, v60, v62, vcc
	global_store_dwordx4 v[58:59], v[42:45], off
	v_pk_fma_f32 v[38:39], v[38:39], s[2:3], v[188:189] op_sel_hi:[1,0,1]
	v_ashrrev_i32_e32 v67, 31, v66
	v_lshl_add_u64 v[42:43], v[68:69], 0, v[106:107]
	global_store_dwordx4 v[42:43], v[46:49], off
	v_pk_fma_f32 v[42:43], v[32:33], s[2:3], v[186:187] op_sel_hi:[1,0,1]
	v_pk_fma_f32 v[44:45], v[30:31], s[2:3], v[184:185] op_sel_hi:[1,0,1]
	v_cndmask_b32_e32 v30, v41, v43, vcc
	v_cndmask_b32_e32 v31, v40, v42, vcc
	v_cndmask_b32_e32 v32, v39, v45, vcc
	v_cndmask_b32_e32 v33, v38, v44, vcc
	v_mov_b32_e32 v46, v1
	v_mov_b32_e32 v47, v1
	v_mov_b32_e32 v48, v1
	v_mov_b32_e32 v49, v1
	v_mov_b32_dpp v46, v33 quad_perm:[1,0,3,2] row_mask:0xf bank_mask:0xf
	v_mov_b32_dpp v47, v32 quad_perm:[1,0,3,2] row_mask:0xf bank_mask:0xf
	v_mov_b32_dpp v48, v31 quad_perm:[1,0,3,2] row_mask:0xf bank_mask:0xf
	v_mov_b32_dpp v49, v30 quad_perm:[1,0,3,2] row_mask:0xf bank_mask:0xf
	v_cndmask_b32_e32 v33, v49, v41, vcc
	v_cndmask_b32_e32 v32, v48, v40, vcc
	v_cndmask_b32_e32 v31, v47, v39, vcc
	v_cndmask_b32_e32 v30, v46, v38, vcc
	v_cndmask_b32_e32 v41, v43, v49, vcc
	v_cndmask_b32_e32 v40, v42, v48, vcc
	v_lshl_add_u64 v[42:43], v[68:69], 0, v[100:101]
	v_cndmask_b32_e32 v39, v45, v47, vcc
	v_cndmask_b32_e32 v38, v44, v46, vcc
	global_store_dwordx4 v[42:43], v[30:33], off
	v_mov_b32_e32 v42, v1
	v_mov_b32_e32 v43, v1
	v_lshl_add_u64 v[30:31], v[68:69], 0, v[98:99]
	global_store_dwordx4 v[30:31], v[38:41], off
	v_lshl_add_u64 v[30:31], v[0:1], 0, v[66:67]
	s_nop 0
	v_pk_fma_f32 v[32:33], v[34:35], s[2:3], v[192:193] op_sel_hi:[1,0,1]
	v_lshl_add_u64 v[38:39], v[30:31], 2, s[0:1]
	v_pk_fma_f32 v[30:31], v[36:37], s[2:3], v[194:195] op_sel_hi:[1,0,1]
	v_pk_fma_f32 v[34:35], v[28:29], s[2:3], v[198:199] op_sel_hi:[1,0,1]
	v_pk_fma_f32 v[36:37], v[26:27], s[2:3], v[196:197] op_sel_hi:[1,0,1]
	v_cndmask_b32_e32 v0, v31, v35, vcc
	v_cndmask_b32_e32 v26, v30, v34, vcc
	v_cndmask_b32_e32 v27, v33, v37, vcc
	v_cndmask_b32_e32 v28, v32, v36, vcc
	v_mov_b32_e32 v40, v1
	v_mov_b32_e32 v41, v1
	v_mov_b32_dpp v42, v26 quad_perm:[1,0,3,2] row_mask:0xf bank_mask:0xf
	v_mov_b32_dpp v40, v28 quad_perm:[1,0,3,2] row_mask:0xf bank_mask:0xf
	v_mov_b32_dpp v41, v27 quad_perm:[1,0,3,2] row_mask:0xf bank_mask:0xf
	v_mov_b32_dpp v43, v0 quad_perm:[1,0,3,2] row_mask:0xf bank_mask:0xf
	v_cndmask_b32_e32 v29, v43, v31, vcc
	v_cndmask_b32_e32 v28, v42, v30, vcc
	v_cndmask_b32_e32 v27, v41, v33, vcc
	v_cndmask_b32_e32 v26, v40, v32, vcc
	v_cndmask_b32_e32 v33, v35, v43, vcc
	v_cndmask_b32_e32 v32, v34, v42, vcc
	v_lshl_add_u64 v[34:35], v[38:39], 0, v[154:155]
	v_cndmask_b32_e32 v31, v37, v41, vcc
	v_cndmask_b32_e32 v30, v36, v40, vcc
	global_store_dwordx4 v[34:35], v[26:29], off offset:128
	v_pk_fma_f32 v[24:25], v[24:25], s[2:3], v[194:195] op_sel_hi:[1,0,1]
	v_pk_fma_f32 v[22:23], v[22:23], s[2:3], v[192:193] op_sel_hi:[1,0,1]
	v_lshl_add_u64 v[26:27], v[38:39], 0, v[152:153]
	global_store_dwordx4 v[26:27], v[30:33], off offset:128
	v_pk_fma_f32 v[26:27], v[20:21], s[2:3], v[198:199] op_sel_hi:[1,0,1]
	v_pk_fma_f32 v[28:29], v[18:19], s[2:3], v[196:197] op_sel_hi:[1,0,1]
	v_cndmask_b32_e32 v0, v25, v27, vcc
	v_cndmask_b32_e32 v18, v24, v26, vcc
	v_cndmask_b32_e32 v19, v23, v29, vcc
	v_cndmask_b32_e32 v20, v22, v28, vcc
	v_mov_b32_e32 v30, v1
	v_mov_b32_e32 v31, v1
	v_mov_b32_e32 v32, v1
	v_mov_b32_e32 v33, v1
	v_mov_b32_dpp v30, v20 quad_perm:[1,0,3,2] row_mask:0xf bank_mask:0xf
	v_mov_b32_dpp v31, v19 quad_perm:[1,0,3,2] row_mask:0xf bank_mask:0xf
	v_mov_b32_dpp v32, v18 quad_perm:[1,0,3,2] row_mask:0xf bank_mask:0xf
	v_mov_b32_dpp v33, v0 quad_perm:[1,0,3,2] row_mask:0xf bank_mask:0xf
	v_cndmask_b32_e32 v21, v33, v25, vcc
	v_cndmask_b32_e32 v20, v32, v24, vcc
	v_cndmask_b32_e32 v19, v31, v23, vcc
	v_cndmask_b32_e32 v18, v30, v22, vcc
	v_cndmask_b32_e32 v25, v27, v33, vcc
	v_cndmask_b32_e32 v24, v26, v32, vcc
	v_lshl_add_u64 v[26:27], v[38:39], 0, v[148:149]
	v_cndmask_b32_e32 v23, v29, v31, vcc
	v_cndmask_b32_e32 v22, v28, v30, vcc
	global_store_dwordx4 v[26:27], v[18:21], off offset:128
	v_pk_fma_f32 v[16:17], v[16:17], s[2:3], v[194:195] op_sel_hi:[1,0,1]
	v_pk_fma_f32 v[14:15], v[14:15], s[2:3], v[192:193] op_sel_hi:[1,0,1]
	v_lshl_add_u64 v[18:19], v[38:39], 0, v[146:147]
	global_store_dwordx4 v[18:19], v[22:25], off offset:128
	v_pk_fma_f32 v[18:19], v[12:13], s[2:3], v[198:199] op_sel_hi:[1,0,1]
	v_pk_fma_f32 v[20:21], v[10:11], s[2:3], v[196:197] op_sel_hi:[1,0,1]
	v_cndmask_b32_e32 v0, v17, v19, vcc
	v_cndmask_b32_e32 v10, v16, v18, vcc
	v_cndmask_b32_e32 v11, v15, v21, vcc
	v_cndmask_b32_e32 v12, v14, v20, vcc
	v_mov_b32_e32 v22, v1
	v_mov_b32_e32 v23, v1
	v_mov_b32_e32 v24, v1
	v_mov_b32_e32 v25, v1
	v_mov_b32_dpp v22, v12 quad_perm:[1,0,3,2] row_mask:0xf bank_mask:0xf
	v_mov_b32_dpp v23, v11 quad_perm:[1,0,3,2] row_mask:0xf bank_mask:0xf
	v_mov_b32_dpp v24, v10 quad_perm:[1,0,3,2] row_mask:0xf bank_mask:0xf
	v_mov_b32_dpp v25, v0 quad_perm:[1,0,3,2] row_mask:0xf bank_mask:0xf
	v_cndmask_b32_e32 v13, v25, v17, vcc
	v_cndmask_b32_e32 v12, v24, v16, vcc
	v_cndmask_b32_e32 v11, v23, v15, vcc
	v_cndmask_b32_e32 v10, v22, v14, vcc
	v_cndmask_b32_e32 v17, v19, v25, vcc
	v_cndmask_b32_e32 v16, v18, v24, vcc
	v_lshl_add_u64 v[18:19], v[38:39], 0, v[108:109]
	v_cndmask_b32_e32 v15, v21, v23, vcc
	v_cndmask_b32_e32 v14, v20, v22, vcc
	global_store_dwordx4 v[18:19], v[10:13], off offset:128
	v_pk_fma_f32 v[8:9], v[8:9], s[2:3], v[194:195] op_sel_hi:[1,0,1]
	v_pk_fma_f32 v[6:7], v[6:7], s[2:3], v[192:193] op_sel_hi:[1,0,1]
	v_lshl_add_u64 v[10:11], v[38:39], 0, v[106:107]
	global_store_dwordx4 v[10:11], v[14:17], off offset:128
	v_pk_fma_f32 v[10:11], v[4:5], s[2:3], v[198:199] op_sel_hi:[1,0,1]
	v_pk_fma_f32 v[12:13], v[2:3], s[2:3], v[196:197] op_sel_hi:[1,0,1]
	v_cndmask_b32_e32 v0, v9, v11, vcc
	v_cndmask_b32_e32 v2, v8, v10, vcc
	v_cndmask_b32_e32 v3, v7, v13, vcc
	v_cndmask_b32_e32 v4, v6, v12, vcc
	v_mov_b32_e32 v14, v1
	v_mov_b32_e32 v15, v1
	v_mov_b32_e32 v16, v1
	v_mov_b32_dpp v14, v4 quad_perm:[1,0,3,2] row_mask:0xf bank_mask:0xf
	v_mov_b32_dpp v15, v3 quad_perm:[1,0,3,2] row_mask:0xf bank_mask:0xf
	v_mov_b32_dpp v16, v2 quad_perm:[1,0,3,2] row_mask:0xf bank_mask:0xf
	v_mov_b32_dpp v1, v0 quad_perm:[1,0,3,2] row_mask:0xf bank_mask:0xf
	v_cndmask_b32_e32 v5, v1, v9, vcc
	v_cndmask_b32_e32 v4, v16, v8, vcc
	v_cndmask_b32_e32 v3, v15, v7, vcc
	v_cndmask_b32_e32 v2, v14, v6, vcc
	v_cndmask_b32_e32 v9, v11, v1, vcc
	v_lshl_add_u64 v[0:1], v[38:39], 0, v[100:101]
	v_cndmask_b32_e32 v8, v10, v16, vcc
	v_cndmask_b32_e32 v7, v13, v15, vcc
	v_cndmask_b32_e32 v6, v12, v14, vcc
	global_store_dwordx4 v[0:1], v[2:5], off offset:128
	v_lshl_add_u64 v[0:1], v[38:39], 0, v[98:99]
	global_store_dwordx4 v[0:1], v[6:9], off offset:128
	s_endpgm

	.amdhsa_kernel _Z6k_gemmILi4EEvPKtS1_PvPKfS4_S4_ii
		.amdhsa_group_segment_fixed_size 1024
		.amdhsa_private_segment_fixed_size 0
		.amdhsa_kernarg_size 56
		.amdhsa_user_sgpr_count 2
		.amdhsa_user_sgpr_dispatch_ptr 0
		.amdhsa_user_sgpr_queue_ptr 0
		.amdhsa_user_sgpr_kernarg_segment_ptr 1
		.amdhsa_user_sgpr_dispatch_id 0
		.amdhsa_user_sgpr_kernarg_preload_length 0
		.amdhsa_user_sgpr_kernarg_preload_offset 0
		.amdhsa_user_sgpr_private_segment_size 0
		.amdhsa_uses_dynamic_stack 0
		.amdhsa_enable_private_segment 0
		.amdhsa_system_sgpr_workgroup_id_x 1
		.amdhsa_system_sgpr_workgroup_id_y 0
		.amdhsa_system_sgpr_workgroup_id_z 0
		.amdhsa_system_sgpr_workgroup_info 0
		.amdhsa_system_vgpr_workitem_id 0
		.amdhsa_next_free_vgpr 256
		.amdhsa_next_free_sgpr 60
		.amdhsa_accum_offset 256
		.amdhsa_reserve_vcc 1
		.amdhsa_float_round_mode_32 0
		.amdhsa_float_round_mode_16_64 0
		.amdhsa_float_denorm_mode_32 3
		.amdhsa_float_denorm_mode_16_64 3
		.amdhsa_dx10_clamp 1
		.amdhsa_ieee_mode 1
		.amdhsa_fp16_overflow 0
		.amdhsa_tg_split 0
		.amdhsa_exception_fp_ieee_invalid_op 0
		.amdhsa_exception_fp_denorm_src 0
		.amdhsa_exception_fp_ieee_div_zero 0
		.amdhsa_exception_fp_ieee_overflow 0
		.amdhsa_exception_fp_ieee_underflow 0
		.amdhsa_exception_fp_ieee_inexact 0
		.amdhsa_exception_int_div_zero 0
	.end_amdhsa_kernel

amdhsa.kernels:
  - .agpr_count:     0
    .args:
      - .actual_access:  read_only
        .address_space:  global
        .offset:         0
        .size:           8
        .value_kind:     global_buffer
      - .actual_access:  write_only
        .address_space:  global
        .offset:         8
        .size:           8
        .value_kind:     global_buffer
      - .offset:         16
        .size:           4
        .value_kind:     by_value
      - .actual_access:  read_only
        .address_space:  global
        .offset:         24
        .size:           8
        .value_kind:     global_buffer
      - .actual_access:  read_only
        .address_space:  global
        .offset:         32
        .size:           8
        .value_kind:     global_buffer
      - .actual_access:  read_only
        .address_space:  global
        .offset:         40
        .size:           8
        .value_kind:     global_buffer
      - .actual_access:  read_only
        .address_space:  global
        .offset:         48
        .size:           8
        .value_kind:     global_buffer
      - .actual_access:  write_only
        .address_space:  global
        .offset:         56
        .size:           8
        .value_kind:     global_buffer
      - .actual_access:  write_only
        .address_space:  global
        .offset:         64
        .size:           8
        .value_kind:     global_buffer
      - .actual_access:  write_only
        .address_space:  global
        .offset:         72
        .size:           8
        .value_kind:     global_buffer
    .group_segment_fixed_size: 16640
    .kernarg_segment_align: 8
    .kernarg_segment_size: 80
    .language:       OpenCL C
    .language_version:
      - 2
      - 0
    .max_flat_workgroup_size: 256
    .name:           _Z6k_prepPK15HIP_vector_typeIfLj4EEPS_IjLj4EEiPKfS6_S6_S6_PtS7_PS_IfLj2EE
    .private_segment_fixed_size: 0
    .sgpr_count:     22
    .sgpr_spill_count: 0
    .symbol:         _Z6k_prepPK15HIP_vector_typeIfLj4EEPS_IjLj4EEiPKfS6_S6_S6_PtS7_PS_IfLj2EE.kd
    .uniform_work_group_size: 1
    .uses_dynamic_stack: false
    .vgpr_count:     45
    .vgpr_spill_count: 0
    .wavefront_size: 64
  - .agpr_count:     0
    .args:
      - .actual_access:  read_only
        .address_space:  global
        .offset:         0
        .size:           8
        .value_kind:     global_buffer
      - .actual_access:  write_only
        .address_space:  global
        .offset:         8
        .size:           8
        .value_kind:     global_buffer
      - .actual_access:  read_only
        .address_space:  global
        .offset:         16
        .size:           8
        .value_kind:     global_buffer
    .group_segment_fixed_size: 36928
    .kernarg_segment_align: 8
    .kernarg_segment_size: 24
    .language:       OpenCL C
    .language_version:
      - 2
      - 0
    .max_flat_workgroup_size: 256
    .name:           _Z5k_fftPKtPtPKDv2_f
    .private_segment_fixed_size: 0
    .sgpr_count:     23
    .sgpr_spill_count: 0
    .symbol:         _Z5k_fftPKtPtPKDv2_f.kd
    .uniform_work_group_size: 1
    .uses_dynamic_stack: false
    .vgpr_count:     128
    .vgpr_spill_count: 0
    .wavefront_size: 64
  - .agpr_count:     0
    .args:
      - .address_space:  global
        .offset:         0
        .size:           8
        .value_kind:     global_buffer
      - .address_space:  global
        .offset:         8
        .size:           8
        .value_kind:     global_buffer
      - .actual_access:  write_only
        .address_space:  global
        .offset:         16
        .size:           8
        .value_kind:     global_buffer
      - .actual_access:  read_only
        .address_space:  global
        .offset:         24
        .size:           8
        .value_kind:     global_buffer
      - .actual_access:  read_only
        .address_space:  global
        .offset:         32
        .size:           8
        .value_kind:     global_buffer
      - .actual_access:  read_only
        .address_space:  global
        .offset:         40
        .size:           8
        .value_kind:     global_buffer
      - .offset:         48
        .size:           4
        .value_kind:     by_value
      - .offset:         52
        .size:           4
        .value_kind:     by_value
    .group_segment_fixed_size: 1024
    .kernarg_segment_align: 8
    .kernarg_segment_size: 56
    .language:       OpenCL C
    .language_version:
      - 2
      - 0
    .max_flat_workgroup_size: 512
    .name:           _Z6k_gemmILi2EEvPKtS1_PvPKfS4_S4_ii
    .private_segment_fixed_size: 0
    .sgpr_count:     96
    .sgpr_spill_count: 0
    .symbol:         _Z6k_gemmILi2EEvPKtS1_PvPKfS4_S4_ii.kd
    .uniform_work_group_size: 1
    .uses_dynamic_stack: false
    .vgpr_count:     256
    .vgpr_spill_count: 0
    .wavefront_size: 64
  - .agpr_count:     0
    .args:
      - .address_space:  global
        .offset:         0
        .size:           8
        .value_kind:     global_buffer
      - .address_space:  global
        .offset:         8
        .size:           8
        .value_kind:     global_buffer
      - .actual_access:  write_only
        .address_space:  global
        .offset:         16
        .size:           8
        .value_kind:     global_buffer
      - .actual_access:  read_only
        .address_space:  global
        .offset:         24
        .size:           8
        .value_kind:     global_buffer
      - .actual_access:  read_only
        .address_space:  global
        .offset:         32
        .size:           8
        .value_kind:     global_buffer
      - .actual_access:  read_only
        .address_space:  global
        .offset:         40
        .size:           8
        .value_kind:     global_buffer
      - .offset:         48
        .size:           4
        .value_kind:     by_value
      - .offset:         52
        .size:           4
        .value_kind:     by_value
    .group_segment_fixed_size: 1024
    .kernarg_segment_align: 8
    .kernarg_segment_size: 56
    .language:       OpenCL C
    .language_version:
      - 2
      - 0
    .max_flat_workgroup_size: 512
    .name:           _Z6k_gemmILi4EEvPKtS1_PvPKfS4_S4_ii
    .private_segment_fixed_size: 0
    .sgpr_count:     66
    .sgpr_spill_count: 0
    .symbol:         _Z6k_gemmILi4EEvPKtS1_PvPKfS4_S4_ii.kd
    .uniform_work_group_size: 1
    .uses_dynamic_stack: false
    .vgpr_count:     256
    .vgpr_spill_count: 0
    .wavefront_size: 64
